# speedup vs baseline: 1.0438x; 1.0109x over previous
.LBB1_1:
	s_add_i32 s12, s12, 2
	s_waitcnt lgkmcnt(2)
	v_mfma_f32_32x32x64_f8f6f4 v[76:91], v[84:91], v[116:123], v[36:51]
	v_cvt_pk_fp8_f32 v132, v161, v163
	v_add_u32_e32 v68, s36, v176
	v_cvt_pk_fp8_f32 v132, v162, v164 op_sel:[0,0,1]
	ds_read_b128 v[162:165], v68 offset:49152
	ds_read_b128 v[166:169], v68 offset:50176
	v_cvt_pk_fp8_f32 v133, v150, v154
	v_cvt_pk_fp8_f32 v133, v152, v157 op_sel:[0,0,1]
	s_lshl_b32 s16, s12, 12
	s_add_i32 s15, s16, 0x3000
	s_add_i32 s17, s14, s33
	s_mov_b32 m0, s17
	s_nop 0
	buffer_load_dwordx4 v174, s[20:23], s15 offen lds
	v_cvt_pk_fp8_f32 v134, v149, v153
	v_cvt_pk_fp8_f32 v134, v151, v156 op_sel:[0,0,1]
	v_cvt_pk_fp8_f32 v135, v155, v159
	v_cvt_pk_fp8_f32 v135, v158, v160 op_sel:[0,0,1]
	v_cvt_pk_fp8_f32 v136, v100, v148
	v_cvt_pk_fp8_f32 v136, v101, v102 op_sel:[0,0,1]
	s_waitcnt lgkmcnt(2)
	v_mfma_f32_32x32x64_f8f6f4 v[92:107], v[92:99], v[116:123], v[36:51]
	ds_read_b128 v[148:151], v68 offset:49664
	ds_read_b128 v[152:155], v68 offset:50688
	v_cvt_pk_fp8_f32 v137, v143, v146
	v_cvt_pk_fp8_f32 v137, v145, v147 op_sel:[0,0,1]
	s_add_i32 s15, s16, 0x1000
	s_add_i32 s17, s13, s34
	s_mov_b32 m0, s17
	s_nop 0
	buffer_load_dwordx4 v174, s[24:27], s15 offen lds
	v_cvt_pk_fp8_f32 v138, v69, v109
	v_cvt_pk_fp8_f32 v138, v108, v142 op_sel:[0,0,1]
	v_cvt_pk_fp8_f32 v139, v110, v144
	v_cvt_pk_fp8_f32 v139, v111, v114 op_sel:[0,0,1]
	s_waitcnt lgkmcnt(2)
	s_nop 0
	v_mfma_f32_32x32x64_f8f6f4 v[4:19], v[162:169], v[132:139], v[4:19]
	v_exp_f32_e32 v142, v76
	v_exp_f32_e32 v143, v77
	v_exp_f32_e32 v144, v78
	v_exp_f32_e32 v145, v79
	v_exp_f32_e32 v146, v80
	v_exp_f32_e32 v147, v81
	v_exp_f32_e32 v156, v82
	v_exp_f32_e32 v157, v83
	v_add_u32_e32 v158, s13, v176
	ds_read_b128 v[108:111], v158
	ds_read_b128 v[112:115], v158 offset:1024
	ds_read_b128 v[52:55], v158 offset:512
	ds_read_b128 v[56:59], v158 offset:1536
	v_exp_f32_e32 v159, v84
	v_exp_f32_e32 v160, v85
	v_mfma_f32_16x16x128_f8f6f4 v[200:203], v[124:131], v[132:139], v[200:203]
	v_exp_f32_e32 v161, v86
	v_exp_f32_e32 v162, v87
	v_exp_f32_e32 v163, v88
	v_exp_f32_e32 v164, v89
	v_exp_f32_e32 v165, v90
	v_exp_f32_e32 v166, v91
	s_waitcnt lgkmcnt(4)
	v_mfma_f32_32x32x64_f8f6f4 v[20:35], v[148:155], v[132:139], v[20:35]
	v_exp_f32_e32 v167, v92
	v_exp_f32_e32 v168, v93
	v_exp_f32_e32 v169, v94
	v_exp_f32_e32 v170, v95
	v_exp_f32_e32 v148, v96
	v_exp_f32_e32 v149, v97
	v_exp_f32_e32 v150, v98
	v_exp_f32_e32 v151, v99
	v_exp_f32_e32 v152, v100
	v_exp_f32_e32 v153, v101
	v_exp_f32_e32 v154, v102
	v_exp_f32_e32 v155, v103
	v_exp_f32_e32 v158, v104
	v_exp_f32_e32 v171, v105
	v_exp_f32_e32 v177, v106
	v_exp_f32_e32 v186, v107
	s_waitcnt vmcnt(2) lgkmcnt(0)
	s_barrier
	s_add_i32 s15, s13, 0x4000
	s_cmpk_lg_u32 s13, 0x8000
	s_cselect_b32 s15, s15, 0
	s_waitcnt lgkmcnt(2)
	v_mfma_f32_32x32x64_f8f6f4 v[84:99], v[108:115], v[116:123], v[36:51]
	v_cvt_pk_fp8_f32 v132, v142, v143
	v_add_u32_e32 v142, s14, v176
	v_cvt_pk_fp8_f32 v132, v144, v145 op_sel:[0,0,1]
	ds_read_b128 v[60:63], v142 offset:49152
	ds_read_b128 v[64:67], v142 offset:50176
	v_cvt_pk_fp8_f32 v133, v146, v147
	v_cvt_pk_fp8_f32 v133, v156, v157 op_sel:[0,0,1]
	s_add_i32 s14, s16, 0x4000
	s_add_i32 s17, s13, s33
	s_mov_b32 m0, s17
	s_nop 0
	buffer_load_dwordx4 v174, s[20:23], s14 offen lds
	v_cvt_pk_fp8_f32 v134, v159, v160
	v_cvt_pk_fp8_f32 v134, v161, v162 op_sel:[0,0,1]
	v_cvt_pk_fp8_f32 v135, v163, v164
	v_cvt_pk_fp8_f32 v135, v165, v166 op_sel:[0,0,1]
	s_waitcnt lgkmcnt(2)
	v_mfma_f32_32x32x64_f8f6f4 v[100:115], v[52:59], v[116:123], v[36:51]
	v_cvt_pk_fp8_f32 v136, v167, v168
	v_cvt_pk_fp8_f32 v136, v169, v170 op_sel:[0,0,1]
	ds_read_b128 v[178:181], v142 offset:49664
	ds_read_b128 v[182:185], v142 offset:50688
	v_cvt_pk_fp8_f32 v137, v148, v149
	v_cvt_pk_fp8_f32 v137, v150, v151 op_sel:[0,0,1]
	s_addk_i32 s16, 0x2000
	s_add_i32 s14, s15, s34
	s_mov_b32 m0, s14
	s_nop 0
	buffer_load_dwordx4 v174, s[24:27], s16 offen lds
	v_cvt_pk_fp8_f32 v138, v152, v153
	v_cvt_pk_fp8_f32 v138, v154, v155 op_sel:[0,0,1]
	v_cvt_pk_fp8_f32 v139, v158, v171
	v_cvt_pk_fp8_f32 v139, v177, v186 op_sel:[0,0,1]
	v_sub_f32_e32 v52, v200, v204
	v_mov_b32_e32 v204, v200
	v_max_f32_e32 v0, v0, v0
	v_max_f32_e32 v0, v0, v52
	s_waitcnt lgkmcnt(2)
	v_mfma_f32_32x32x64_f8f6f4 v[4:19], v[60:67], v[132:139], v[4:19]
	v_exp_f32_e32 v161, v84
	v_exp_f32_e32 v163, v85
	v_exp_f32_e32 v162, v86
	v_exp_f32_e32 v164, v87
	v_exp_f32_e32 v150, v88
	v_exp_f32_e32 v154, v89
	v_exp_f32_e32 v152, v90
	v_exp_f32_e32 v157, v91
	v_add_u32_e32 v141, s15, v176
	ds_read_b128 v[84:87], v141
	ds_read_b128 v[88:91], v141 offset:1024
	v_mfma_f32_16x16x128_f8f6f4 v[200:203], v[124:131], v[132:139], v[200:203]
	v_exp_f32_e32 v149, v92
	v_exp_f32_e32 v153, v93
	v_exp_f32_e32 v151, v94
	v_exp_f32_e32 v156, v95
	v_exp_f32_e32 v155, v96
	v_exp_f32_e32 v159, v97
	v_exp_f32_e32 v158, v98
	v_exp_f32_e32 v160, v99
	ds_read_b128 v[92:95], v141 offset:512
	ds_read_b128 v[96:99], v141 offset:1536
	s_waitcnt lgkmcnt(4)
	v_mfma_f32_32x32x64_f8f6f4 v[20:35], v[178:185], v[132:139], v[20:35]
	v_exp_f32_e32 v100, v100
	v_exp_f32_e32 v148, v101
	v_exp_f32_e32 v101, v102
	v_exp_f32_e32 v102, v103
	v_exp_f32_e32 v143, v104
	v_exp_f32_e32 v146, v105
	v_exp_f32_e32 v145, v106
	v_exp_f32_e32 v147, v107
	v_exp_f32_e32 v69, v108
	v_exp_f32_e32 v109, v109
	v_exp_f32_e32 v108, v110
	v_exp_f32_e32 v142, v111
	v_exp_f32_e32 v110, v112
	v_exp_f32_e32 v144, v113
	v_exp_f32_e32 v111, v114
	v_exp_f32_e32 v114, v115
	s_waitcnt vmcnt(2) lgkmcnt(0)
	s_barrier
	s_add_i32 s16, s15, 0x4000
	s_cmpk_lg_u32 s15, 0x8000
	s_mov_b32 s36, s13
	s_mov_b32 s14, s15
	s_cselect_b32 s13, s16, 0
	s_cmp_gt_u32 s12, 24
	s_cbranch_scc0 .LBB1_1
	s_and_b32 s41, s2, 3
	s_lshl_b32 s42, s41, 6
	s_lshl_b32 s43, s3, 5
	s_add_i32 s42, s42, s43
	v_add_u32_e32 v198, s42, v172
	v_lshlrev_b32_e32 v198, 8, v198
	v_lshl_add_u32 v198, v175, 4, v198
	s_lshl_b32 s44, s41, 8
	s_lshl_b32 s45, s3, 7
	s_add_i32 s44, s44, s45
	v_lshl_add_u32 v199, v175, 4, s44
	s_lshl_b32 s46, s41, 2
	v_mov_b32_e32 v205, s46
	v_add_u32_e32 v113, 0xc000, v176
	v_mov_b32_e32 v112, 0x7f7f7f7f
	v_cvt_pk_fp8_f32 v132, v161, v163
	v_cvt_pk_fp8_f32 v132, v162, v164 op_sel:[0,0,1]
	s_waitcnt lgkmcnt(2)
	v_mfma_f32_32x32x64_f8f6f4 v[70:85], v[84:91], v[116:123], v[36:51]
	ds_read_b128 v[162:165], v113 offset:32768
	ds_read_b128 v[166:169], v113 offset:33792
	v_cvt_pk_fp8_f32 v133, v150, v154
	v_cvt_pk_fp8_f32 v133, v152, v157 op_sel:[0,0,1]
	s_mov_b32 s13, 0x1e000
	s_mov_b32 m0, s33
	s_nop 0
	buffer_load_dwordx4 v174, s[20:23], s13 offen lds
	v_cvt_pk_fp8_f32 v134, v149, v153
	v_cvt_pk_fp8_f32 v134, v151, v156 op_sel:[0,0,1]
	v_cvt_pk_fp8_f32 v135, v155, v159
	v_cvt_pk_fp8_f32 v135, v158, v160 op_sel:[0,0,1]
	v_cvt_pk_fp8_f32 v136, v100, v148
	v_cvt_pk_fp8_f32 v136, v101, v102 op_sel:[0,0,1]
	s_waitcnt lgkmcnt(2)
	v_mfma_f32_32x32x64_f8f6f4 v[86:101], v[92:99], v[116:123], v[36:51]
	ds_read_b128 v[148:151], v113 offset:33280
	ds_read_b128 v[152:155], v113 offset:34304
	v_cvt_pk_fp8_f32 v137, v143, v146
	v_cvt_pk_fp8_f32 v137, v145, v147 op_sel:[0,0,1]
	s_cmp_lg_u32 0, -1
	s_cselect_b32 s12, 0, 0
	s_add_i32 s15, s12, s35
	s_add_i32 s12, s15, 0x10000
	s_mov_b32 s26, s22
	s_mov_b32 s27, s23
	s_mov_b32 s14, 0x1c000
	s_mov_b32 m0, s12
	s_nop 0
	buffer_load_dwordx4 v174, s[24:27], s14 offen lds
	global_load_dwordx4 v[208:211], v198, s[4:5]
	global_load_dwordx4 v[212:215], v198, s[4:5] offset:32
	global_load_dwordx4 v[216:219], v198, s[4:5] offset:64
	global_load_dwordx4 v[220:223], v198, s[4:5] offset:96
	global_load_dwordx4 v[224:227], v198, s[4:5] offset:128
	v_cvt_pk_fp8_f32 v138, v69, v109
	v_cvt_pk_fp8_f32 v138, v108, v142 op_sel:[0,0,1]
	v_cvt_pk_fp8_f32 v139, v110, v144
	v_cvt_pk_fp8_f32 v139, v111, v114 op_sel:[0,0,1]
	s_waitcnt lgkmcnt(2)
	s_nop 0
	v_mfma_f32_32x32x64_f8f6f4 v[4:19], v[162:169], v[132:139], v[4:19]
	v_exp_f32_e32 v104, v73
	v_exp_f32_e32 v69, v70
	v_exp_f32_e32 v102, v71
	v_exp_f32_e32 v103, v72
	v_exp_f32_e32 v110, v74
	v_exp_f32_e32 v111, v75
	v_exp_f32_e32 v114, v76
	v_exp_f32_e32 v115, v77
	ds_read_b128 v[70:73], v176 offset:16384
	ds_read_b128 v[74:77], v176 offset:17408
	v_mfma_f32_16x16x128_f8f6f4 v[200:203], v[124:131], v[132:139], v[200:203]
	v_exp_f32_e32 v140, v78
	v_exp_f32_e32 v141, v79
	v_exp_f32_e32 v142, v80
	v_exp_f32_e32 v143, v81
	v_exp_f32_e32 v144, v82
	v_exp_f32_e32 v145, v83
	v_exp_f32_e32 v146, v84
	v_exp_f32_e32 v147, v85
	s_waitcnt lgkmcnt(2)
	v_mfma_f32_32x32x64_f8f6f4 v[20:35], v[148:155], v[132:139], v[20:35]
	v_exp_f32_e32 v156, v86
	v_exp_f32_e32 v157, v87
	v_exp_f32_e32 v158, v88
	v_exp_f32_e32 v159, v89
	v_exp_f32_e32 v148, v90
	v_exp_f32_e32 v149, v91
	v_exp_f32_e32 v150, v92
	v_exp_f32_e32 v151, v93
	ds_read_b128 v[86:89], v176 offset:16896
	ds_read_b128 v[90:93], v176 offset:17920
	v_exp_f32_e32 v152, v94
	v_exp_f32_e32 v153, v95
	v_exp_f32_e32 v154, v96
	v_exp_f32_e32 v155, v97
	v_exp_f32_e32 v160, v98
	v_exp_f32_e32 v161, v99
	v_exp_f32_e32 v162, v100
	v_exp_f32_e32 v163, v101
	s_waitcnt vmcnt(7) lgkmcnt(0)
	s_barrier
	s_waitcnt lgkmcnt(2)
	v_mfma_f32_32x32x64_f8f6f4 v[70:85], v[70:77], v[116:123], v[36:51]
	v_cvt_pk_fp8_f32 v132, v69, v102
	v_cvt_pk_fp8_f32 v132, v103, v104 op_sel:[0,0,1]
	ds_read_b128 v[102:105], v176 offset:49152
	ds_read_b128 v[106:109], v176 offset:50176
	v_cvt_pk_fp8_f32 v133, v110, v111
	v_cvt_pk_fp8_f32 v133, v114, v115 op_sel:[0,0,1]
	s_add_i32 s16, s15, 0x4000
	s_mov_b32 s14, 0x1f000
	s_mov_b32 m0, s16
	s_nop 0
	buffer_load_dwordx4 v174, s[20:23], s14 offen lds
	v_cvt_pk_fp8_f32 v134, v140, v141
	v_cvt_pk_fp8_f32 v134, v142, v143 op_sel:[0,0,1]
	v_cvt_pk_fp8_f32 v135, v144, v145
	v_cvt_pk_fp8_f32 v135, v146, v147 op_sel:[0,0,1]
	s_waitcnt lgkmcnt(2)
	v_mfma_f32_32x32x64_f8f6f4 v[86:101], v[86:93], v[116:123], v[36:51]
	v_cvt_pk_fp8_f32 v136, v156, v157
	v_cvt_pk_fp8_f32 v136, v158, v159 op_sel:[0,0,1]
	ds_read_b128 v[140:143], v176 offset:49664
	ds_read_b128 v[144:147], v176 offset:50688
	v_cvt_pk_fp8_f32 v137, v148, v149
	v_cvt_pk_fp8_f32 v137, v150, v151 op_sel:[0,0,1]
	s_add_i32 s15, s15, 0x14000
	s_mov_b32 s16, 0x1d000
	s_mov_b32 m0, s15
	s_nop 0
	buffer_load_dwordx4 v174, s[24:27], s16 offen lds
	global_load_dwordx4 v[228:231], v198, s[4:5] offset:160
	global_load_dwordx4 v[232:235], v198, s[4:5] offset:192
	global_load_dwordx4 v[236:239], v198, s[4:5] offset:224
	global_load_dwordx4 v[240:243], v199, s[6:7]
	v_cvt_pk_fp8_f32 v138, v152, v153
	v_cvt_pk_fp8_f32 v138, v154, v155 op_sel:[0,0,1]
	v_cvt_pk_fp8_f32 v139, v160, v161
	v_cvt_pk_fp8_f32 v139, v162, v163 op_sel:[0,0,1]
	v_sub_f32_e32 v114, v200, v204
	v_mov_b32_e32 v204, v200
	s_waitcnt lgkmcnt(2)
	v_mfma_f32_32x32x64_f8f6f4 v[4:19], v[102:109], v[132:139], v[4:19]
	v_exp_f32_e32 v110, v70
	v_exp_f32_e32 v111, v71
	v_exp_f32_e32 v148, v73
	v_exp_f32_e32 v115, v72
	v_exp_f32_e32 v149, v74
	v_exp_f32_e32 v150, v75
	v_exp_f32_e32 v151, v76
	v_exp_f32_e32 v152, v77
	ds_read_b128 v[70:73], v176 offset:32768
	ds_read_b128 v[74:77], v176 offset:33792
	v_mfma_f32_16x16x128_f8f6f4 v[200:203], v[124:131], v[132:139], v[200:203]
	v_exp_f32_e32 v153, v78
	v_exp_f32_e32 v154, v79
	v_exp_f32_e32 v155, v80
	v_exp_f32_e32 v156, v81
	v_exp_f32_e32 v157, v83
	v_exp_f32_e32 v158, v84
	v_exp_f32_e32 v159, v85
	s_nop 7
	v_exp_f32_e32 v53, v82
	s_waitcnt lgkmcnt(2)
	v_mfma_f32_32x32x64_f8f6f4 v[20:35], v[140:147], v[132:139], v[20:35]
	v_exp_f32_e32 v160, v86
	v_exp_f32_e32 v161, v87
	v_exp_f32_e32 v162, v88
	v_exp_f32_e32 v163, v89
	v_exp_f32_e32 v164, v90
	v_exp_f32_e32 v165, v91
	v_exp_f32_e32 v166, v92
	v_exp_f32_e32 v167, v93
	ds_read_b128 v[78:81], v176 offset:33280
	ds_read_b128 v[82:85], v176 offset:34304
	v_exp_f32_e32 v168, v94
	v_exp_f32_e32 v169, v95
	v_exp_f32_e32 v170, v96
	v_exp_f32_e32 v171, v97
	v_exp_f32_e32 v177, v98
	v_exp_f32_e32 v178, v99
	v_exp_f32_e32 v179, v100
	v_exp_f32_e32 v180, v101
	s_waitcnt vmcnt(11) lgkmcnt(0)
	s_barrier
	s_waitcnt lgkmcnt(2)
	v_mfma_f32_32x32x64_f8f6f4 v[86:101], v[70:77], v[116:123], v[36:51]
	v_cvt_pk_fp8_f32 v132, v110, v111
	v_cvt_pk_fp8_f32 v132, v115, v148 op_sel:[0,0,1]
	ds_read_b128 v[102:105], v113 offset:16384
	ds_read_b128 v[106:109], v113 offset:17408
	v_cvt_pk_fp8_f32 v133, v149, v150
	v_cvt_pk_fp8_f32 v133, v151, v152 op_sel:[0,0,1]
	v_cvt_pk_fp8_f32 v134, v153, v154
	v_cvt_pk_fp8_f32 v134, v155, v156 op_sel:[0,0,1]
	v_cvt_pk_fp8_f32 v135, v53, v157
	v_cvt_pk_fp8_f32 v135, v158, v159 op_sel:[0,0,1]
	s_waitcnt lgkmcnt(2)
	v_mfma_f32_32x32x64_f8f6f4 v[70:85], v[78:85], v[116:123], v[36:51]
	v_cvt_pk_fp8_f32 v136, v160, v161
	v_cvt_pk_fp8_f32 v136, v162, v163 op_sel:[0,0,1]
	ds_read_b128 v[140:143], v113 offset:16896
	ds_read_b128 v[144:147], v113 offset:17920
	v_cvt_pk_fp8_f32 v137, v164, v165
	v_cvt_pk_fp8_f32 v137, v166, v167 op_sel:[0,0,1]
	s_mov_b32 m0, s34
	s_nop 0
	buffer_load_dwordx4 v174, s[24:27], s13 offen lds
	global_load_dwordx4 v[244:247], v199, s[6:7] offset:32
	global_load_dwordx4 v[248:251], v199, s[6:7] offset:64
	global_load_dwordx4 v[252:255], v199, s[6:7] offset:96
	global_load_dword v205, v205, s[8:9]
	v_cvt_pk_fp8_f32 v138, v168, v169
	v_cvt_pk_fp8_f32 v138, v170, v171 op_sel:[0,0,1]
	v_cvt_pk_fp8_f32 v139, v177, v178
	v_cvt_pk_fp8_f32 v139, v179, v180 op_sel:[0,0,1]
	s_waitcnt lgkmcnt(2)
	s_nop 0
	v_mfma_f32_32x32x64_f8f6f4 v[4:19], v[102:109], v[132:139], v[4:19]
	v_exp_f32_e32 v148, v88
	v_exp_f32_e32 v149, v89
	v_exp_f32_e32 v53, v86
	v_exp_f32_e32 v115, v87
	v_exp_f32_e32 v150, v92
	v_exp_f32_e32 v151, v93
	v_exp_f32_e32 v102, v90
	v_exp_f32_e32 v103, v91
	ds_read_b128 v[86:89], v176
	ds_read_b128 v[90:93], v176 offset:1024
	v_mfma_f32_16x16x128_f8f6f4 v[200:203], v[124:131], v[132:139], v[200:203]
	v_exp_f32_e32 v152, v94
	v_exp_f32_e32 v153, v95
	v_exp_f32_e32 v154, v96
	v_exp_f32_e32 v155, v97
	v_exp_f32_e32 v156, v98
	v_exp_f32_e32 v157, v99
	v_exp_f32_e32 v158, v100
	v_exp_f32_e32 v159, v101
	s_waitcnt lgkmcnt(2)
	v_mfma_f32_32x32x64_f8f6f4 v[20:35], v[140:147], v[132:139], v[20:35]
	v_exp_f32_e32 v160, v70
	v_exp_f32_e32 v161, v71
	v_exp_f32_e32 v162, v72
	v_exp_f32_e32 v163, v73
	v_exp_f32_e32 v164, v74
	v_exp_f32_e32 v165, v75
	v_exp_f32_e32 v166, v76
	v_exp_f32_e32 v167, v77
	ds_read_b128 v[94:97], v176 offset:512
	ds_read_b128 v[98:101], v176 offset:1536
	v_exp_f32_e32 v168, v78
	v_exp_f32_e32 v169, v79
	v_exp_f32_e32 v170, v80
	v_exp_f32_e32 v171, v81
	v_exp_f32_e32 v177, v82
	v_exp_f32_e32 v178, v83
	v_exp_f32_e32 v179, v84
	v_exp_f32_e32 v180, v85
	s_waitcnt vmcnt(9) lgkmcnt(0)
	s_barrier
	s_waitcnt lgkmcnt(2)
	v_mfma_f32_32x32x64_f8f6f4 v[70:85], v[86:93], v[116:123], v[36:51]
	ds_read_b128 v[104:107], v113 offset:32768
	ds_read_b128 v[108:111], v113 offset:33792
	v_cvt_pk_fp8_f32 v132, v53, v115
	v_cvt_pk_fp8_f32 v133, v102, v103
	v_cvt_pk_fp8_f32 v134, v152, v153
	v_cvt_pk_fp8_f32 v132, v148, v149 op_sel:[0,0,1]
	v_cvt_pk_fp8_f32 v133, v150, v151 op_sel:[0,0,1]
	v_cvt_pk_fp8_f32 v134, v154, v155 op_sel:[0,0,1]
	v_cvt_pk_fp8_f32 v135, v156, v157
	v_cvt_pk_fp8_f32 v135, v158, v159 op_sel:[0,0,1]
	s_waitcnt lgkmcnt(2)
	v_mfma_f32_32x32x64_f8f6f4 v[86:101], v[94:101], v[116:123], v[36:51]
	v_cvt_pk_fp8_f32 v136, v160, v161
	v_cvt_pk_fp8_f32 v136, v162, v163 op_sel:[0,0,1]
	ds_read_b128 v[140:143], v113 offset:33280
	ds_read_b128 v[144:147], v113 offset:34304
	v_cvt_pk_fp8_f32 v137, v164, v165
	v_cvt_pk_fp8_f32 v137, v166, v167 op_sel:[0,0,1]
	s_mov_b32 m0, s12
	s_nop 0
	buffer_load_dwordx4 v174, s[24:27], s14 offen lds
	v_cvt_pk_fp8_f32 v138, v168, v169
	v_cvt_pk_fp8_f32 v138, v170, v171 op_sel:[0,0,1]
	v_cvt_pk_fp8_f32 v139, v177, v178
	v_cvt_pk_fp8_f32 v139, v179, v180 op_sel:[0,0,1]
	v_sub_f32_e32 v52, v200, v204
	v_mov_b32_e32 v204, v200
	v_max3_f32 v0, v0, v114, v52
	v_exp_f32_e32 v72, v72
	v_exp_f32_e32 v73, v73
	v_exp_f32_e32 v52, v70
	v_exp_f32_e32 v53, v71
	v_exp_f32_e32 v102, v74
	v_exp_f32_e32 v103, v75
	v_exp_f32_e32 v114, v76
	v_exp_f32_e32 v115, v77
	ds_read_b128 v[150:153], v176 offset:16384
	ds_read_b128 v[154:157], v176 offset:17408
	v_mfma_f32_16x16x128_f8f6f4 v[200:203], v[124:131], v[132:139], v[200:203]
	v_exp_f32_e32 v177, v78
	v_exp_f32_e32 v178, v79
	v_exp_f32_e32 v179, v80
	v_exp_f32_e32 v180, v81
	s_nop 10
	v_exp_f32_e32 v55, v82
	v_exp_f32_e32 v181, v83
	v_exp_f32_e32 v182, v84
	v_exp_f32_e32 v183, v85
	v_exp_f32_e32 v184, v86
	v_exp_f32_e32 v185, v87
	v_exp_f32_e32 v88, v88
	v_exp_f32_e32 v89, v89
	v_exp_f32_e32 v186, v90
	v_exp_f32_e32 v187, v91
	v_exp_f32_e32 v188, v92
	v_exp_f32_e32 v189, v93
	ds_read_b128 v[164:167], v176 offset:16896
	ds_read_b128 v[168:171], v176 offset:17920
	v_exp_f32_e32 v190, v94
	v_exp_f32_e32 v191, v95
	v_exp_f32_e32 v192, v96
	v_exp_f32_e32 v193, v97
	v_exp_f32_e32 v194, v98
	v_exp_f32_e32 v195, v99
	v_exp_f32_e32 v196, v100
	v_exp_f32_e32 v197, v101
	s_waitcnt vmcnt(0) lgkmcnt(0)
	s_barrier
	v_mov_b32_e32 v148, v132
	v_cvt_pk_fp8_f32 v148, v52, v53
	v_cvt_pk_fp8_f32 v148, v72, v73 op_sel:[0,0,1]
	s_waitcnt lgkmcnt(2)
	v_mfma_f32_32x32x64_f8f6f4 v[72:87], v[150:157], v[116:123], v[36:51]
	ds_read_b128 v[156:159], v176 offset:49152
	ds_read_b128 v[160:163], v176 offset:50176
	v_mov_b32_e32 v149, v133
	v_cvt_pk_fp8_f32 v149, v102, v103
	v_cvt_pk_fp8_f32 v149, v114, v115 op_sel:[0,0,1]
	v_mov_b32_e32 v150, v134
	v_cvt_pk_fp8_f32 v150, v177, v178
	v_cvt_pk_fp8_f32 v150, v179, v180 op_sel:[0,0,1]
	v_mov_b32_e32 v151, v135
	v_cvt_pk_fp8_f32 v151, v55, v181
	v_cvt_pk_fp8_f32 v151, v182, v183 op_sel:[0,0,1]
	v_mov_b32_e32 v152, v136
	v_cvt_pk_fp8_f32 v152, v184, v185
	v_cvt_pk_fp8_f32 v152, v88, v89 op_sel:[0,0,1]
	s_waitcnt lgkmcnt(2)
	v_mfma_f32_32x32x64_f8f6f4 v[88:103], v[164:171], v[116:123], v[36:51]
	ds_read_b128 v[164:167], v176 offset:49664
	ds_read_b128 v[168:171], v176 offset:50688
	v_mov_b32_e32 v153, v137
	v_cvt_pk_fp8_f32 v153, v186, v187
	v_cvt_pk_fp8_f32 v153, v188, v189 op_sel:[0,0,1]
	v_mov_b32_e32 v154, v138
	v_cvt_pk_fp8_f32 v154, v190, v191
	v_cvt_pk_fp8_f32 v154, v192, v193 op_sel:[0,0,1]
	v_mov_b32_e32 v155, v139
	v_cvt_pk_fp8_f32 v155, v194, v195
	v_cvt_pk_fp8_f32 v155, v196, v197 op_sel:[0,0,1]
	v_sub_f32_e32 v52, v200, v204
	v_mov_b32_e32 v204, v200
	s_nop 2
	v_exp_f32_e32 v36, v72
	v_exp_f32_e32 v37, v73
	v_exp_f32_e32 v38, v74
	v_exp_f32_e32 v39, v75
	v_exp_f32_e32 v40, v76
	v_exp_f32_e32 v41, v77
	v_exp_f32_e32 v42, v78
	v_exp_f32_e32 v43, v79
	v_exp_f32_e32 v53, v80
	v_exp_f32_e32 v80, v83
	v_exp_f32_e32 v54, v81
	v_exp_f32_e32 v55, v82
	v_exp_f32_e32 v81, v84
	v_exp_f32_e32 v82, v85
	v_exp_f32_e32 v83, v86
	v_exp_f32_e32 v84, v87
	v_exp_f32_e32 v44, v88
	v_exp_f32_e32 v45, v89
	v_exp_f32_e32 v46, v90
	v_exp_f32_e32 v47, v91
	v_exp_f32_e32 v48, v92
	v_exp_f32_e32 v49, v93
	v_exp_f32_e32 v50, v94
	v_exp_f32_e32 v51, v95
	v_exp_f32_e32 v75, v96
	v_exp_f32_e32 v85, v97
	v_exp_f32_e32 v86, v98
	v_exp_f32_e32 v87, v99
	v_exp_f32_e32 v88, v100
	v_exp_f32_e32 v89, v101
	v_exp_f32_e32 v90, v102
	v_exp_f32_e32 v91, v103
	v_mov_b32_e32 v72, 0
	v_mov_b32_e32 v76, 0
	v_mov_b32_e32 v73, 0
	v_mov_b32_e32 v77, 0
	v_cvt_pk_fp8_f32 v72, v36, v37
	v_cvt_pk_fp8_f32 v76, v44, v45
	v_cvt_pk_fp8_f32 v73, v40, v41
	v_cvt_pk_fp8_f32 v77, v48, v49
	v_cvt_pk_fp8_f32 v72, v38, v39 op_sel:[0,0,1]
	v_cvt_pk_fp8_f32 v76, v46, v47 op_sel:[0,0,1]
	v_cvt_pk_fp8_f32 v73, v42, v43 op_sel:[0,0,1]
	v_cvt_pk_fp8_f32 v77, v50, v51 op_sel:[0,0,1]
	v_mfma_f32_16x16x128_f8f6f4 v[200:203], v[124:131], v[148:155], v[200:203]
	v_mov_b32_e32 v78, 0
	v_mov_b32_e32 v79, 0
	v_mov_b32_e32 v74, 0
	v_cvt_pk_fp8_f32 v78, v75, v85
	v_mov_b32_e32 v75, 0
	v_cvt_pk_fp8_f32 v74, v53, v54
	v_cvt_pk_fp8_f32 v75, v81, v82
	v_cvt_pk_fp8_f32 v79, v88, v89
	v_cvt_pk_fp8_f32 v78, v86, v87 op_sel:[0,0,1]
	v_cvt_pk_fp8_f32 v74, v55, v80 op_sel:[0,0,1]
	v_cvt_pk_fp8_f32 v75, v83, v84 op_sel:[0,0,1]
	v_cvt_pk_fp8_f32 v79, v90, v91 op_sel:[0,0,1]
	ds_read_b128 v[80:83], v113 offset:16384
	s_nop 1
	ds_read_b128 v[58:61], v113 offset:16896
	ds_read_b128 v[84:87], v113 offset:17408
	ds_read_b128 v[62:65], v113 offset:17920
	s_mov_b32 s12, 0x43c80000
	v_mfma_f32_16x16x128_f8f6f4 v[200:203], v[124:131], v[72:79], v[200:203]
	s_nop 15
	s_nop 3
	v_sub_f32_e32 v37, v200, v204
	v_max3_f32 v0, v0, v52, v37
	v_cmp_nge_f32_e32 vcc, s12, v0
	s_cmp_lg_u64 vcc, 0
	s_cselect_b64 s[12:13], -1, 0
	s_cbranch_vccz .LBB1_12
	v_mfma_f32_32x32x64_f8f6f4 v[4:19], v[104:111], v[132:139], v[4:19]
	s_andn2_b64 vcc, exec, s[12:13]
	v_mfma_f32_32x32x64_f8f6f4 v[20:35], v[140:147], v[132:139], v[20:35]
	s_cbranch_vccnz .LBB1_5

.LBB1_11:
	s_lshl_b32 s0, s30, 5
	s_lshl_b32 s1, s31, 7
	s_and_b32 s13, s2, 3
	s_or_b32 s14, s0, s1
	s_lshl_b32 s0, s3, 5
	s_lshl_b32 s12, s13, 6
	s_add_i32 s1, s0, s12
	v_or_b32_e32 v36, s1, v172
	v_mov_b32_e32 v37, 0
	s_lshl_b32 s2, s13, 8
	v_lshlrev_b64 v[0:1], 8, v[36:37]
	s_add_u32 s2, s6, s2
	v_lshl_add_u64 v[0:1], s[4:5], 0, v[0:1]
	v_lshlrev_b32_e32 v36, 4, v175
	s_addc_u32 s4, s7, 0
	s_lshl_b32 s3, s3, 7
	v_lshl_add_u64 v[8:9], v[0:1], 0, v[36:37]
	s_add_u32 s2, s2, s3
	s_addc_u32 s3, s4, 0
	v_lshl_add_u64 v[10:11], v[8:9], 0, 32
	v_lshl_add_u64 v[10:11], s[2:3], 0, v[36:37]
	v_lshl_add_u64 v[12:13], v[8:9], 0, 64
	s_mov_b64 s[2:3], 0x60
	v_lshl_add_u64 v[12:13], v[8:9], 0, s[2:3]
	v_lshl_add_u64 v[12:13], v[10:11], 0, 32
	s_mov_b64 s[4:5], 0x80
	v_lshl_add_u64 v[12:13], v[8:9], 0, s[4:5]
	s_mov_b64 s[4:5], 0xa0
	v_lshl_add_u64 v[12:13], v[8:9], 0, s[4:5]
	v_lshl_add_u64 v[12:13], v[10:11], 0, 64
	s_mov_b64 s[4:5], 0xc0
	v_lshl_add_u64 v[12:13], v[8:9], 0, s[4:5]
	s_mov_b64 s[4:5], 0xe0
	v_lshl_add_u64 v[8:9], v[8:9], 0, s[4:5]
	v_lshl_add_u64 v[8:9], v[10:11], 0, s[2:3]
	s_lshl_b32 s2, s28, 20
	s_mov_b32 s1, 0
	s_add_u32 s4, s18, s2
	s_addc_u32 s5, s19, 0
	s_lshl_b64 s[2:3], s[0:1], 14
	s_add_u32 s4, s4, s2
	s_mov_b32 s15, s1
	s_addc_u32 s5, s5, s3
	s_lshl_b64 s[2:3], s[14:15], 2
	s_add_u32 s4, s4, s2
	s_addc_u32 s5, s5, s3
	v_lshlrev_b32_e32 v36, 2, v172
	v_lshl_add_u64 v[8:9], s[4:5], 0, v[36:37]
	v_lshlrev_b32_e32 v122, 16, v175
	v_mov_b32_e32 v123, v37
	v_lshl_add_u64 v[8:9], v[8:9], 0, v[122:123]
	s_mov_b64 s[4:5], 0x4000
	global_load_dword v140, v[8:9], off
	v_lshl_add_u64 v[10:11], v[8:9], 0, s[4:5]
	s_mov_b64 s[4:5], 0x8000
	global_load_dword v139, v[10:11], off
	v_lshl_add_u64 v[10:11], v[8:9], 0, s[4:5]
	s_mov_b64 s[4:5], 0xc000
	global_load_dword v138, v[10:11], off
	v_lshl_add_u64 v[10:11], v[8:9], 0, s[4:5]
	s_mov_b64 s[4:5], 0x20000
	global_load_dword v137, v[10:11], off
	v_lshl_add_u64 v[10:11], v[8:9], 0, s[4:5]
	s_mov_b64 s[4:5], 0x24000
	global_load_dword v136, v[10:11], off
	v_lshl_add_u64 v[10:11], v[8:9], 0, s[4:5]
	s_mov_b64 s[4:5], 0x28000
	global_load_dword v135, v[10:11], off
	v_lshl_add_u64 v[10:11], v[8:9], 0, s[4:5]
	s_mov_b64 s[4:5], 0x2c000
	global_load_dword v134, v[10:11], off
	v_lshl_add_u64 v[10:11], v[8:9], 0, s[4:5]
	s_mov_b64 s[4:5], 0x40000
	global_load_dword v133, v[10:11], off
	v_lshl_add_u64 v[10:11], v[8:9], 0, s[4:5]
	s_mov_b64 s[4:5], 0x44000
	global_load_dword v132, v[10:11], off
	v_lshl_add_u64 v[10:11], v[8:9], 0, s[4:5]
	s_mov_b64 s[4:5], 0x48000
	global_load_dword v131, v[10:11], off
	v_lshl_add_u64 v[10:11], v[8:9], 0, s[4:5]
	s_mov_b64 s[4:5], 0x4c000
	global_load_dword v130, v[10:11], off
	v_lshl_add_u64 v[10:11], v[8:9], 0, s[4:5]
	s_mov_b64 s[4:5], 0x60000
	global_load_dword v129, v[10:11], off
	v_lshl_add_u64 v[10:11], v[8:9], 0, s[4:5]
	s_mov_b64 s[4:5], 0x64000
	global_load_dword v128, v[10:11], off
	v_lshl_add_u64 v[10:11], v[8:9], 0, s[4:5]
	s_mov_b64 s[4:5], 0x68000
	global_load_dword v127, v[10:11], off
	v_lshl_add_u64 v[10:11], v[8:9], 0, s[4:5]
	s_mov_b64 s[4:5], 0x6c000
	v_lshl_add_u64 v[8:9], v[8:9], 0, s[4:5]
	s_lshl_b32 s4, s13, 2
	s_add_u32 s4, s8, s4
	global_load_dword v126, v[10:11], off
	s_addc_u32 s5, s9, 0
	global_load_dword v124, v[8:9], off
	v_mov_b64_e32 v[8:9], s[4:5]
	s_mul_i32 s4, s29, 0x2200
	s_add_i32 s4, s4, 0
	v_mov_b32_e32 v8, v141
	v_add_u32_e32 v9, s4, v173
	s_xor_b32 s4, s29, 4
	v_permlane32_swap_b32_e32 v141, v8
	s_mulk_i32 s4, 0x2200
	v_add_f32_e32 v8, v141, v8
	s_add_i32 s4, s4, 0
	ds_write2st64_b32 v9, v146, v8 offset1:1
	ds_write2st64_b32 v9, v54, v55 offset0:2 offset1:3
	ds_write2st64_b32 v9, v38, v39 offset0:18 offset1:19
	ds_write2st64_b32 v9, v56, v57 offset0:4 offset1:5
	ds_write2st64_b32 v9, v40, v41 offset0:20 offset1:21
	ds_write2st64_b32 v9, v58, v59 offset0:6 offset1:7
	ds_write2st64_b32 v9, v42, v43 offset0:22 offset1:23
	ds_write2st64_b32 v9, v60, v61 offset0:8 offset1:9
	ds_write2st64_b32 v9, v44, v45 offset0:24 offset1:25
	ds_write2st64_b32 v9, v62, v63 offset0:10 offset1:11
	ds_write2st64_b32 v9, v46, v47 offset0:26 offset1:27
	ds_write2st64_b32 v9, v64, v65 offset0:12 offset1:13
	ds_write2st64_b32 v9, v48, v49 offset0:28 offset1:29
	ds_write2st64_b32 v9, v66, v67 offset0:14 offset1:15
	ds_write2st64_b32 v9, v50, v51 offset0:30 offset1:31
	ds_write2st64_b32 v9, v68, v69 offset0:16 offset1:17
	ds_write2st64_b32 v9, v52, v53 offset0:32 offset1:33
	v_add_u32_e32 v66, s4, v173
	s_waitcnt lgkmcnt(0)
	s_barrier
	ds_read2st64_b32 v[10:11], v66 offset1:1
	ds_read2st64_b32 v[12:13], v66 offset0:2 offset1:3
	ds_read2st64_b32 v[14:15], v66 offset0:4 offset1:5
	ds_read2st64_b32 v[38:39], v66 offset0:6 offset1:7
	v_max_f32_e32 v40, v146, v146
	s_waitcnt lgkmcnt(3)
	v_max_f32_e32 v9, v10, v10
	v_max_f32_e32 v9, v40, v9
	v_sub_f32_e32 v40, v146, v9
	v_sub_f32_e32 v9, v10, v9
	v_exp_f32_e32 v40, v40
	v_exp_f32_e32 v41, v9
	v_mov_b32_e32 v9, v11
	v_pk_mul_f32 v[8:9], v[8:9], v[40:41]
	s_nop 0
	v_add_f32_e32 v8, v8, v9
	v_div_scale_f32 v9, s[4:5], v8, v8, 1.0
	v_rcp_f32_e32 v10, v9
	s_nop 0
	v_fma_f32 v11, -v9, v10, 1.0
	v_fmac_f32_e32 v10, v11, v10
	v_div_scale_f32 v11, vcc, 1.0, v8, 1.0
	v_mul_f32_e32 v42, v11, v10
	v_fma_f32 v43, -v9, v42, v11
	v_fmac_f32_e32 v42, v43, v10
	v_fma_f32 v9, -v9, v42, v11
	v_div_fmas_f32 v9, v9, v10, v42
	v_div_fixup_f32 v9, v9, v8, 1.0
	v_mul_f32_e32 v8, v40, v9
	v_mul_f32_e32 v10, v41, v9
	ds_read2st64_b32 v[40:41], v66 offset0:18 offset1:19
	ds_read2st64_b32 v[42:43], v66 offset0:20 offset1:21
	ds_read2st64_b32 v[44:45], v66 offset0:22 offset1:23
	ds_read2st64_b32 v[46:47], v66 offset0:16 offset1:17
	s_waitcnt lgkmcnt(6)
	v_pk_mul_f32 v[12:13], v[10:11], v[12:13] op_sel_hi:[0,1]
	s_waitcnt lgkmcnt(5)
	v_pk_mul_f32 v[14:15], v[10:11], v[14:15] op_sel_hi:[0,1]
	s_waitcnt lgkmcnt(4)
	v_pk_mul_f32 v[38:39], v[10:11], v[38:39] op_sel_hi:[0,1]
	s_waitcnt lgkmcnt(3)
	v_pk_mul_f32 v[40:41], v[10:11], v[40:41] op_sel_hi:[0,1]
	v_pk_fma_f32 v[48:49], v[8:9], v[70:71], v[40:41] op_sel_hi:[0,1,1]
	s_waitcnt lgkmcnt(2)
	v_pk_mul_f32 v[40:41], v[10:11], v[42:43] op_sel_hi:[0,1]
	v_pk_fma_f32 v[50:51], v[8:9], v[72:73], v[40:41] op_sel_hi:[0,1,1]
	s_waitcnt lgkmcnt(1)
	v_pk_mul_f32 v[40:41], v[10:11], v[44:45] op_sel_hi:[0,1]
	v_pk_fma_f32 v[52:53], v[8:9], v[74:75], v[40:41] op_sel_hi:[0,1,1]
	ds_read2st64_b32 v[40:41], v66 offset0:8 offset1:9
	ds_read2st64_b32 v[42:43], v66 offset0:24 offset1:25
	ds_read2st64_b32 v[44:45], v66 offset0:10 offset1:11
	ds_read2st64_b32 v[54:55], v66 offset0:12 offset1:13
	ds_read2st64_b32 v[56:57], v66 offset0:14 offset1:15
	ds_read2st64_b32 v[58:59], v66 offset0:26 offset1:27
	ds_read2st64_b32 v[60:61], v66 offset0:28 offset1:29
	ds_read2st64_b32 v[62:63], v66 offset0:30 offset1:31
	s_waitcnt lgkmcnt(6)
	v_pk_mul_f32 v[42:43], v[10:11], v[42:43] op_sel_hi:[0,1]
	v_pk_fma_f32 v[64:65], v[8:9], v[76:77], v[42:43] op_sel_hi:[0,1,1]
	s_waitcnt lgkmcnt(5)
	v_pk_mul_f32 v[42:43], v[10:11], v[44:45] op_sel_hi:[0,1]
	s_waitcnt lgkmcnt(2)
	v_pk_mul_f32 v[44:45], v[10:11], v[58:59] op_sel_hi:[0,1]
	v_pk_fma_f32 v[58:59], v[8:9], v[78:79], v[44:45] op_sel_hi:[0,1,1]
	v_pk_mul_f32 v[44:45], v[10:11], v[54:55] op_sel_hi:[0,1]
	s_waitcnt lgkmcnt(1)
	v_pk_mul_f32 v[54:55], v[10:11], v[60:61] op_sel_hi:[0,1]
	ds_read2st64_b32 v[60:61], v66 offset0:32 offset1:33
	s_waitcnt vmcnt(0)
	v_pk_mul_f32 v[40:41], v[10:11], v[40:41] op_sel_hi:[0,1]
	v_cvt_pk_bf16_f32 v0, v208, v209
	v_cvt_pk_bf16_f32 v1, v210, v211
	v_cvt_pk_bf16_f32 v2, v212, v213
	v_cvt_pk_bf16_f32 v3, v214, v215
	v_pk_fma_f32 v[12:13], v[8:9], v[86:87], v[12:13] op_sel_hi:[0,1,1]
	v_pk_fma_f32 v[14:15], v[8:9], v[88:89], v[14:15] op_sel_hi:[0,1,1]
	v_pk_fma_f32 v[38:39], v[8:9], v[90:91], v[38:39] op_sel_hi:[0,1,1]
	v_pk_fma_f32 v[40:41], v[8:9], v[92:93], v[40:41] op_sel_hi:[0,1,1]
	v_pk_mul_f32 v[56:57], v[10:11], v[56:57] op_sel_hi:[0,1]
	s_waitcnt lgkmcnt(1)
	v_pk_mul_f32 v[62:63], v[10:11], v[62:63] op_sel_hi:[0,1]
	v_pk_mul_f32 v[46:47], v[10:11], v[46:47] op_sel_hi:[0,1]
	s_waitcnt lgkmcnt(0)
	v_pk_mul_f32 v[10:11], v[10:11], v[60:61] op_sel_hi:[0,1]
	v_cvt_pk_bf16_f32 v4, v12, v13
	v_cvt_pk_bf16_f32 v5, v14, v15
	v_cvt_pk_bf16_f32 v6, v38, v39
	v_cvt_pk_bf16_f32 v7, v40, v41
	v_pk_fma_f32 v[42:43], v[8:9], v[94:95], v[42:43] op_sel_hi:[0,1,1]
	v_pk_fma_f32 v[44:45], v[8:9], v[96:97], v[44:45] op_sel_hi:[0,1,1]
	v_pk_fma_f32 v[54:55], v[8:9], v[80:81], v[54:55] op_sel_hi:[0,1,1]
	v_pk_fma_f32 v[56:57], v[8:9], v[98:99], v[56:57] op_sel_hi:[0,1,1]
	v_pk_fma_f32 v[62:63], v[8:9], v[82:83], v[62:63] op_sel_hi:[0,1,1]
	v_pk_fma_f32 v[46:47], v[8:9], v[100:101], v[46:47] op_sel_hi:[0,1,1]
	v_pk_fma_f32 v[60:61], v[8:9], v[84:85], v[10:11] op_sel_hi:[0,1,1]
	v_mfma_f32_32x32x16_bf16 v[0:15], v[0:3], v[4:7], 0
	v_cvt_pk_bf16_f32 v42, v42, v43
	v_cvt_pk_bf16_f32 v38, v216, v217
	v_cvt_pk_bf16_f32 v39, v218, v219
	v_cvt_pk_bf16_f32 v40, v220, v221
	v_cvt_pk_bf16_f32 v41, v222, v223
	v_cvt_pk_bf16_f32 v43, v44, v45
	v_cvt_pk_bf16_f32 v44, v56, v57
	v_cvt_pk_bf16_f32 v45, v46, v47
	s_nop 1
	v_mfma_f32_32x32x16_bf16 v[0:15], v[38:41], v[42:45], v[0:15]
	v_cvt_pk_bf16_f32 v38, v224, v225
	v_cvt_pk_bf16_f32 v39, v226, v227
	v_cvt_pk_bf16_f32 v40, v228, v229
	v_cvt_pk_bf16_f32 v41, v230, v231
	v_cvt_pk_bf16_f32 v42, v48, v49
	v_cvt_pk_bf16_f32 v43, v50, v51
	v_cvt_pk_bf16_f32 v44, v52, v53
	v_cvt_pk_bf16_f32 v45, v64, v65
	v_cvt_pk_bf16_f32 v32, v232, v233
	v_cvt_pk_bf16_f32 v33, v234, v235
	v_mfma_f32_32x32x16_bf16 v[0:15], v[38:41], v[42:45], v[0:15]
	v_cvt_pk_bf16_f32 v34, v236, v237
	v_cvt_pk_bf16_f32 v35, v238, v239
	v_cvt_pk_bf16_f32 v38, v58, v59
	v_add_f32_e32 v42, 1.0, v205
	v_div_scale_f32 v43, s[4:5], v42, v42, 1.0
	v_rcp_f32_e32 v44, v43
	v_cvt_pk_bf16_f32 v39, v54, v55
	v_cvt_pk_bf16_f32 v40, v62, v63
	v_cvt_pk_bf16_f32 v41, v60, v61
	s_lshl_b32 s4, s28, 8
	s_or_b32 s4, s4, s12
	v_mfma_f32_32x32x16_bf16 v[0:15], v[32:35], v[38:41], v[0:15]
	v_fma_f32 v32, -v43, v44, 1.0
	v_fmac_f32_e32 v44, v32, v44
	v_div_scale_f32 v32, vcc, 1.0, v42, 1.0
	s_add_i32 s0, s4, s0
	v_mul_f32_e32 v33, v32, v44
	s_lshl_b64 s[0:1], s[0:1], 14
	v_fma_f32 v34, -v43, v33, v32
	s_add_u32 s0, s10, s0
	v_fmac_f32_e32 v33, v34, v44
	s_addc_u32 s1, s11, s1
	v_fma_f32 v32, -v43, v33, v32
	s_add_u32 s0, s0, s2
	v_div_fmas_f32 v32, v32, v44, v33
	s_addc_u32 s1, s1, s3
	v_add_f32_e32 v0, v0, v240
	v_div_fixup_f32 v34, v32, v42, 1.0
	v_lshl_add_u64 v[32:33], s[0:1], 0, v[36:37]
	v_fmac_f32_e32 v140, v205, v0
	v_mul_f32_e32 v0, v34, v140
	v_lshl_add_u64 v[32:33], v[32:33], 0, v[122:123]
	global_store_dword v[32:33], v0, off
	v_add_f32_e32 v0, v1, v241
	s_movk_i32 s0, 0x4000
	v_fmac_f32_e32 v139, v205, v0
	v_add_co_u32_e32 v0, vcc, s0, v32
	v_mul_f32_e32 v28, v34, v139
	s_nop 0
	v_addc_co_u32_e32 v1, vcc, 0, v33, vcc
	global_store_dword v[0:1], v28, off
	v_add_f32_e32 v0, v2, v242
	s_mov_b32 s0, 0x8000
	v_fmac_f32_e32 v138, v205, v0
	v_add_co_u32_e32 v0, vcc, s0, v32
	v_mul_f32_e32 v2, v34, v138
	s_nop 0
	v_addc_co_u32_e32 v1, vcc, 0, v33, vcc
	global_store_dword v[0:1], v2, off
	v_add_f32_e32 v0, v3, v243
	s_mov_b32 s0, 0xc000
	v_fmac_f32_e32 v137, v205, v0
	v_add_co_u32_e32 v0, vcc, s0, v32
	v_mul_f32_e32 v2, v34, v137
	s_nop 0
	v_addc_co_u32_e32 v1, vcc, 0, v33, vcc
	global_store_dword v[0:1], v2, off
	v_add_f32_e32 v0, v4, v244
	s_mov_b32 s0, 0x20000
	v_fmac_f32_e32 v136, v205, v0
	v_add_co_u32_e32 v0, vcc, s0, v32
	v_mul_f32_e32 v2, v34, v136
	s_nop 0
	v_addc_co_u32_e32 v1, vcc, 0, v33, vcc
	global_store_dword v[0:1], v2, off
	v_add_f32_e32 v0, v5, v245
	s_mov_b32 s0, 0x24000
	v_fmac_f32_e32 v135, v205, v0
	v_add_co_u32_e32 v0, vcc, s0, v32
	v_mul_f32_e32 v2, v34, v135
	s_nop 0
	v_addc_co_u32_e32 v1, vcc, 0, v33, vcc
	global_store_dword v[0:1], v2, off
	v_add_f32_e32 v0, v6, v246
	s_mov_b32 s0, 0x28000
	v_fmac_f32_e32 v134, v205, v0
	v_add_co_u32_e32 v0, vcc, s0, v32
	v_mul_f32_e32 v2, v34, v134
	s_nop 0
	v_addc_co_u32_e32 v1, vcc, 0, v33, vcc
	global_store_dword v[0:1], v2, off
	v_add_f32_e32 v0, v7, v247
	s_mov_b32 s0, 0x2c000
	v_fmac_f32_e32 v133, v205, v0
	v_add_co_u32_e32 v0, vcc, s0, v32
	v_mul_f32_e32 v2, v34, v133
	s_nop 0
	v_addc_co_u32_e32 v1, vcc, 0, v33, vcc
	global_store_dword v[0:1], v2, off
	v_add_f32_e32 v0, v8, v248
	s_mov_b32 s0, 0x40000
	v_fmac_f32_e32 v132, v205, v0
	v_add_co_u32_e32 v0, vcc, s0, v32
	v_mul_f32_e32 v2, v34, v132
	s_nop 0
	v_addc_co_u32_e32 v1, vcc, 0, v33, vcc
	global_store_dword v[0:1], v2, off
	v_add_f32_e32 v0, v9, v249
	s_mov_b32 s0, 0x44000
	v_fmac_f32_e32 v131, v205, v0
	v_add_co_u32_e32 v0, vcc, s0, v32
	v_mul_f32_e32 v2, v34, v131
	s_nop 0
	v_addc_co_u32_e32 v1, vcc, 0, v33, vcc
	global_store_dword v[0:1], v2, off
	v_add_f32_e32 v0, v10, v250
	s_mov_b32 s0, 0x48000
	v_fmac_f32_e32 v130, v205, v0
	v_add_co_u32_e32 v0, vcc, s0, v32
	v_mul_f32_e32 v2, v34, v130
	s_nop 0
	v_addc_co_u32_e32 v1, vcc, 0, v33, vcc
	global_store_dword v[0:1], v2, off
	v_add_f32_e32 v0, v11, v251
	s_mov_b32 s0, 0x4c000
	v_fmac_f32_e32 v129, v205, v0
	v_add_co_u32_e32 v0, vcc, s0, v32
	v_mul_f32_e32 v2, v34, v129
	s_nop 0
	v_addc_co_u32_e32 v1, vcc, 0, v33, vcc
	global_store_dword v[0:1], v2, off
	v_add_f32_e32 v0, v12, v252
	s_mov_b32 s0, 0x60000
	v_fmac_f32_e32 v128, v205, v0
	v_add_co_u32_e32 v0, vcc, s0, v32
	v_mul_f32_e32 v2, v34, v128
	s_nop 0
	v_addc_co_u32_e32 v1, vcc, 0, v33, vcc
	global_store_dword v[0:1], v2, off
	v_add_f32_e32 v0, v13, v253
	s_mov_b32 s0, 0x64000
	v_fmac_f32_e32 v127, v205, v0
	v_add_co_u32_e32 v0, vcc, s0, v32
	v_mul_f32_e32 v2, v34, v127
	s_nop 0
	v_addc_co_u32_e32 v1, vcc, 0, v33, vcc
	global_store_dword v[0:1], v2, off
	v_add_f32_e32 v0, v14, v254
	s_mov_b32 s0, 0x68000
	v_fmac_f32_e32 v126, v205, v0
	v_add_co_u32_e32 v0, vcc, s0, v32
	v_mul_f32_e32 v2, v34, v126
	s_nop 0
	v_addc_co_u32_e32 v1, vcc, 0, v33, vcc
	global_store_dword v[0:1], v2, off
	v_add_f32_e32 v0, v15, v255
	v_fmac_f32_e32 v124, v205, v0
	v_add_co_u32_e32 v0, vcc, 0x6c000, v32
	v_mul_f32_e32 v2, v34, v124
	s_nop 0
	v_addc_co_u32_e32 v1, vcc, 0, v33, vcc
	global_store_dword v[0:1], v2, off
	s_endpgm

	.amdhsa_kernel _Z11attn_kernelPKfS0_S0_PKcS2_PKDv4_jS0_S0_S0_S0_Pf
		.amdhsa_group_segment_fixed_size 0
		.amdhsa_private_segment_fixed_size 0
		.amdhsa_kernarg_size 88
		.amdhsa_user_sgpr_count 2
		.amdhsa_user_sgpr_dispatch_ptr 0
		.amdhsa_user_sgpr_queue_ptr 0
		.amdhsa_user_sgpr_kernarg_segment_ptr 1
		.amdhsa_user_sgpr_dispatch_id 0
		.amdhsa_user_sgpr_kernarg_preload_length 0
		.amdhsa_user_sgpr_kernarg_preload_offset 0
		.amdhsa_user_sgpr_private_segment_size 0
		.amdhsa_uses_dynamic_stack 0
		.amdhsa_enable_private_segment 0
		.amdhsa_system_sgpr_workgroup_id_x 1
		.amdhsa_system_sgpr_workgroup_id_y 0
		.amdhsa_system_sgpr_workgroup_id_z 0
		.amdhsa_system_sgpr_workgroup_info 0
		.amdhsa_system_vgpr_workitem_id 0
		.amdhsa_next_free_vgpr 256
		.amdhsa_next_free_sgpr 47
		.amdhsa_accum_offset 256
		.amdhsa_reserve_vcc 1
		.amdhsa_float_round_mode_32 0
		.amdhsa_float_round_mode_16_64 0
		.amdhsa_float_denorm_mode_32 3
		.amdhsa_float_denorm_mode_16_64 3
		.amdhsa_dx10_clamp 1
		.amdhsa_ieee_mode 1
		.amdhsa_fp16_overflow 0
		.amdhsa_tg_split 0
		.amdhsa_exception_fp_ieee_invalid_op 0
		.amdhsa_exception_fp_denorm_src 0
		.amdhsa_exception_fp_ieee_div_zero 0
		.amdhsa_exception_fp_ieee_overflow 0
		.amdhsa_exception_fp_ieee_underflow 0
		.amdhsa_exception_fp_ieee_inexact 0
		.amdhsa_exception_int_div_zero 0
	.end_amdhsa_kernel

amdhsa.kernels:
  - .agpr_count:     32
    .args:
      - .actual_access:  read_only
        .address_space:  global
        .offset:         0
        .size:           8
        .value_kind:     global_buffer
      - .actual_access:  read_only
        .address_space:  global
        .offset:         8
        .size:           8
        .value_kind:     global_buffer
      - .actual_access:  read_only
        .address_space:  global
        .offset:         16
        .size:           8
        .value_kind:     global_buffer
      - .actual_access:  read_only
        .address_space:  global
        .offset:         24
        .size:           8
        .value_kind:     global_buffer
      - .actual_access:  read_only
        .address_space:  global
        .offset:         32
        .size:           8
        .value_kind:     global_buffer
      - .actual_access:  read_only
        .address_space:  global
        .offset:         40
        .size:           8
        .value_kind:     global_buffer
      - .actual_access:  read_only
        .address_space:  global
        .offset:         48
        .size:           8
        .value_kind:     global_buffer
      - .actual_access:  write_only
        .address_space:  global
        .offset:         56
        .size:           8
        .value_kind:     global_buffer
      - .actual_access:  write_only
        .address_space:  global
        .offset:         64
        .size:           8
        .value_kind:     global_buffer
      - .actual_access:  write_only
        .address_space:  global
        .offset:         72
        .size:           8
        .value_kind:     global_buffer
      - .actual_access:  write_only
        .address_space:  global
        .offset:         80
        .size:           8
        .value_kind:     global_buffer
      - .actual_access:  write_only
        .address_space:  global
        .offset:         88
        .size:           8
        .value_kind:     global_buffer
      - .actual_access:  write_only
        .address_space:  global
        .offset:         96
        .size:           8
        .value_kind:     global_buffer
      - .actual_access:  write_only
        .address_space:  global
        .offset:         104
        .size:           8
        .value_kind:     global_buffer
    .group_segment_fixed_size: 18944
    .kernarg_segment_align: 8
    .kernarg_segment_size: 112
    .language:       OpenCL C
    .language_version:
      - 2
      - 0
    .max_flat_workgroup_size: 256
    .name:           _Z11prep_kernelPKfS0_S0_S0_S0_S0_S0_PDv4_jS2_S2_PfS3_S3_S3_
    .private_segment_fixed_size: 0
    .sgpr_count:     24
    .sgpr_spill_count: 0
    .symbol:         _Z11prep_kernelPKfS0_S0_S0_S0_S0_S0_PDv4_jS2_S2_PfS3_S3_S3_.kd
    .uniform_work_group_size: 1
    .uses_dynamic_stack: false
    .vgpr_count:     132
    .vgpr_spill_count: 0
    .wavefront_size: 64
  - .agpr_count:     0
    .args:
      - .address_space:  global
        .offset:         0
        .size:           8
        .value_kind:     global_buffer
      - .address_space:  global
        .offset:         8
        .size:           8
        .value_kind:     global_buffer
      - .address_space:  global
        .offset:         16
        .size:           8
        .value_kind:     global_buffer
      - .address_space:  global
        .offset:         24
        .size:           8
        .value_kind:     global_buffer
      - .address_space:  global
        .offset:         32
        .size:           8
        .value_kind:     global_buffer
      - .actual_access:  read_only
        .address_space:  global
        .offset:         40
        .size:           8
        .value_kind:     global_buffer
      - .actual_access:  read_only
        .address_space:  global
        .offset:         48
        .size:           8
        .value_kind:     global_buffer
      - .address_space:  global
        .offset:         56
        .size:           8
        .value_kind:     global_buffer
      - .actual_access:  read_only
        .address_space:  global
        .offset:         64
        .size:           8
        .value_kind:     global_buffer
      - .actual_access:  read_only
        .address_space:  global
        .offset:         72
        .size:           8
        .value_kind:     global_buffer
      - .actual_access:  write_only
        .address_space:  global
        .offset:         80
        .size:           8
        .value_kind:     global_buffer
    .group_segment_fixed_size: 0
    .kernarg_segment_align: 8
    .kernarg_segment_size: 88
    .language:       OpenCL C
    .language_version:
      - 2
      - 0
    .max_flat_workgroup_size: 512
    .name:           _Z11attn_kernelPKfS0_S0_PKcS2_PKDv4_jS0_S0_S0_S0_Pf
    .private_segment_fixed_size: 0
    .sgpr_count:     53
    .sgpr_spill_count: 0
    .symbol:         _Z11attn_kernelPKfS0_S0_PKcS2_PKDv4_jS0_S0_S0_S0_Pf.kd
    .uniform_work_group_size: 1
    .uses_dynamic_stack: false
    .vgpr_count:     256
    .vgpr_spill_count: 0
    .wavefront_size: 64
